# speedup vs baseline: 1.0117x; 1.0014x over previous
.LBB0_3:
	s_load_dwordx8 s[20:27], s[0:1], 0x68
	v_and_b32_e32 v2, 31, v0
	s_lshr_b32 s3, s2, 3
	s_and_b32 s30, s2, 7
	v_cmp_gt_u32_e64 s[10:11], 21, v2
	s_mul_i32 s30, s30, 0x30000
	v_lshrrev_b32_e32 v6, 5, v0
	v_cndmask_b32_e64 v1, 0, v2, s[10:11]
	s_cmpk_gt_u32 s2, 0x41f
	s_cbranch_scc0 .LBB0_11
	s_cmpk_gt_u32 s2, 0x45f
	s_cbranch_scc0 .LBB0_8
	s_load_dwordx2 s[28:29], s[0:1], 0x60
	s_load_dwordx2 s[18:19], s[0:1], 0x48
	s_load_dwordx2 s[8:9], s[0:1], 0x38
	s_load_dwordx2 s[32:33], s[0:1], 0x40
	s_load_dwordx4 s[36:39], s[0:1], 0x50
	v_lshrrev_b32_e32 v3, 2, v2
	v_and_b32_e32 v2, 28, v2
	v_and_b32_e32 v7, 3, v0
	v_and_b32_e32 v51, 7, v0
	v_lshlrev_b32_e32 v51, 2, v51
	s_waitcnt lgkmcnt(0)
	global_load_dword v52, v51, s[28:29]
	global_load_dword v53, v51, s[32:33]
	global_load_dword v54, v51, s[38:39]
	global_load_dword v55, v51, s[36:37]
	global_load_dword v51, v51, s[18:19]
	global_load_dword v22, v2, s[18:19]
	global_load_dword v23, v2, s[28:29]
	v_cmp_lt_u32_e32 vcc, 31, v0
	v_mul_u32_u24_e32 v24, 27, v3
	v_sub_u32_e32 v27, 2, v7
	v_cndmask_b32_e64 v2, 0, 1, vcc
	v_sub_co_u32_e32 v26, vcc, 1, v7
	v_max_i32_e32 v8, 0, v26
	v_lshl_add_u32 v8, v8, 3, v8
	v_sub_u32_e32 v16, 4, v7
	v_add_lshl_u32 v4, v24, v2, 2
	v_mov_b32_e32 v5, 0
	v_ashrrev_i32_e32 v9, 31, v8
	v_max_i32_e32 v12, 0, v27
	v_min_u32_e32 v16, 2, v16
	v_lshl_add_u64 v[2:3], s[8:9], 0, v[4:5]
	v_lshlrev_b64 v[8:9], 2, v[8:9]
	v_mul_u32_u24_e32 v12, 9, v12
	v_mul_u32_u24_e32 v16, 9, v16
	v_lshl_add_u64 v[10:11], v[2:3], 0, v[8:9]
	v_lshlrev_b32_e32 v12, 2, v12
	v_mov_b32_e32 v13, v5
	v_lshlrev_b32_e32 v16, 2, v16
	v_mov_b32_e32 v17, v5
	global_load_dword v25, v4, s[8:9]
	v_lshl_add_u64 v[14:15], v[2:3], 0, v[12:13]
	v_lshl_add_u64 v[18:19], v[2:3], 0, v[16:17]
	global_load_dword v28, v[10:11], off
	global_load_dword v29, v[14:15], off
	global_load_dword v30, v[18:19], off
	v_bitop3_b32 v10, v0, 3, v0 bitop3:0xc
	v_min_u32_e32 v10, 2, v10
	v_mul_u32_u24_e32 v10, 9, v10
	v_lshlrev_b32_e32 v10, 2, v10
	v_mov_b32_e32 v11, v5
	v_lshl_add_u64 v[2:3], v[2:3], 0, v[10:11]
	v_cmp_gt_u32_e64 s[4:5], 32, v0
	global_load_dword v31, v[2:3], off
	global_load_dword v32, v4, s[8:9] offset:72
	v_cndmask_b32_e64 v2, 4, 3, s[4:5]
	v_add_lshl_u32 v4, v2, v24, 2
	v_lshl_add_u64 v[2:3], s[8:9], 0, v[4:5]
	v_lshl_add_u64 v[14:15], v[2:3], 0, v[8:9]
	global_load_dword v33, v4, s[8:9]
	global_load_dword v34, v[14:15], off
	v_lshl_add_u64 v[14:15], v[2:3], 0, v[12:13]
	v_lshl_add_u64 v[18:19], v[2:3], 0, v[10:11]
	v_lshl_add_u64 v[2:3], v[2:3], 0, v[16:17]
	global_load_dword v35, v[14:15], off
	global_load_dword v36, v[18:19], off
	global_load_dword v37, v[2:3], off
	global_load_dword v38, v4, s[8:9] offset:72
	v_cndmask_b32_e64 v2, 8, 7, s[4:5]
	v_add_lshl_u32 v4, v2, v24, 2
	v_lshl_add_u64 v[2:3], s[8:9], 0, v[4:5]
	v_lshl_add_u64 v[14:15], v[2:3], 0, v[8:9]
	v_lshl_add_u64 v[18:19], v[2:3], 0, v[12:13]
	v_lshl_add_u64 v[20:21], v[2:3], 0, v[10:11]
	v_lshl_add_u64 v[2:3], v[2:3], 0, v[16:17]
	global_load_dword v39, v4, s[8:9]
	global_load_dword v40, v[14:15], off
	global_load_dword v41, v[18:19], off
	global_load_dword v42, v[20:21], off
	global_load_dword v43, v[2:3], off
	global_load_dword v44, v4, s[8:9] offset:72
	v_cndmask_b32_e64 v2, 5, 2, s[4:5]
	v_add_lshl_u32 v4, v2, v24, 2
	v_lshl_add_u64 v[2:3], s[8:9], 0, v[4:5]
	v_lshl_add_u64 v[14:15], v[2:3], 0, v[8:9]
	v_lshl_add_u64 v[18:19], v[2:3], 0, v[12:13]
	v_lshl_add_u64 v[20:21], v[2:3], 0, v[10:11]
	v_lshl_add_u64 v[2:3], v[2:3], 0, v[16:17]
	global_load_dword v45, v[14:15], off
	global_load_dword v46, v[18:19], off
	global_load_dword v47, v[20:21], off
	global_load_dword v48, v[2:3], off
	global_load_dword v49, v4, s[8:9]
	global_load_dword v50, v4, s[8:9] offset:72
	v_cndmask_b32_e64 v2, 8, 6, s[4:5]
	v_add_lshl_u32 v4, v2, v24, 2
	s_mov_b32 s31, 0x800000
	v_lshl_add_u64 v[2:3], s[8:9], 0, v[4:5]
	v_lshl_add_u64 v[8:9], v[2:3], 0, v[8:9]
	v_lshl_add_u64 v[12:13], v[2:3], 0, v[12:13]
	v_lshl_add_u64 v[10:11], v[2:3], 0, v[10:11]
	v_lshl_add_u64 v[2:3], v[2:3], 0, v[16:17]
	v_cmp_gt_u32_e64 s[12:13], 3, v27
	v_cmp_ne_u32_e64 s[14:15], 0, v7
	v_cmp_eq_u32_e64 s[16:17], 3, v7
	s_add_u32 s24, s24, s30
	s_addc_u32 s25, s25, 0
	global_load_dword v15, v4, s[8:9]
	global_load_dword v16, v[8:9], off
	global_load_dword v17, v[12:13], off
	global_load_dword v18, v[10:11], off
	global_load_dword v19, v4, s[8:9] offset:72
	global_load_dword v20, v[2:3], off
	s_mov_b32 s34, 0xe52632a
	v_writelane_b32 v56, s34, 0
	s_mov_b32 s34, 0x2102e45
	v_writelane_b32 v56, s34, 1
	s_mov_b32 s34, 0x1f202f6f
	v_writelane_b32 v56, s34, 2
	s_mov_b32 s34, 0x142d0a56
	v_writelane_b32 v56, s34, 3
	s_mov_b32 s34, 0x2b1c1160
	v_writelane_b32 v56, s34, 4
	s_mov_b32 s34, 0x47394854
	v_writelane_b32 v56, s34, 5
	s_mov_b32 s34, 0x12071303
	v_writelane_b32 v56, s34, 6
	s_mov_b32 s34, 0x15746465
	v_writelane_b32 v56, s34, 7
	s_mov_b32 s34, 0x2b5a3e22
	v_writelane_b32 v56, s34, 8
	s_mov_b32 s34, 0x34176831
	v_writelane_b32 v56, s34, 9
	s_mov_b32 s34, 0x50354d33
	v_writelane_b32 v56, s34, 10
	s_mov_b32 s34, 0x1b43114f
	v_writelane_b32 v56, s34, 11
	s_mov_b32 s34, 0x3d66413c
	v_writelane_b32 v56, s34, 12
	s_mov_b32 s34, 0x9235c30
	v_writelane_b32 v56, s34, 13
	s_mov_b32 s34, 0x40695d59
	v_writelane_b32 v56, s34, 14
	s_mov_b32 s34, 0x5e361a4e
	v_writelane_b32 v56, s34, 15
	s_mov_b32 s34, 0x1441d
	v_writelane_b32 v56, s34, 16
	s_mov_b32 s34, 0x46625370
	v_writelane_b32 v56, s34, 17
	s_mov_b32 s34, 0x572c1e3b
	v_writelane_b32 v56, s34, 18
	s_mov_b32 s34, 0x72054b4a
	v_writelane_b32 v56, s34, 19
	s_mov_b32 s34, 0xf37616e
	v_writelane_b32 v56, s34, 20
	s_mov_b32 s34, 0x4376171
	v_writelane_b32 v56, s34, 21
	s_mov_b32 s34, 0x49373821
	v_writelane_b32 v56, s34, 22
	s_mov_b32 s34, 0x4c735516
	v_writelane_b32 v56, s34, 23
	s_mov_b32 s34, 0x25763a77
	v_writelane_b32 v56, s34, 24
	s_mov_b32 s34, 0x266a5827
	v_writelane_b32 v56, s34, 25
	s_mov_b32 s34, 0x190b676c
	v_writelane_b32 v56, s34, 26
	s_mov_b32 s34, 0xd51296d
	v_writelane_b32 v56, s34, 27
	s_mov_b32 s34, 0x8067524
	v_writelane_b32 v56, s34, 28
	s_mov_b32 s34, 0x323f4418
	v_writelane_b32 v56, s34, 29
	s_mov_b32 s34, 0x5b780c42
	v_writelane_b32 v56, s34, 30
	s_mov_b32 s34, 0x6b285f1d
	v_writelane_b32 v56, s34, 31
	s_mov_b32 s34, 0x38587000
	v_writelane_b32 v57, s34, 0
	s_mov_b32 s34, 0xa878
	v_writelane_b32 v58, s34, 0
	s_mov_b32 s34, 0x80482830
	v_writelane_b32 v57, s34, 1
	s_mov_b32 s34, 0xa068
	v_writelane_b32 v58, s34, 1
	s_mov_b32 s34, 0x59790191
	v_writelane_b32 v57, s34, 2
	s_mov_b32 s34, 0x3971
	v_writelane_b32 v58, s34, 2
	s_mov_b32 s34, 0x9949515a
	v_writelane_b32 v57, s34, 3
	s_mov_b32 s34, 0x2969
	v_writelane_b32 v58, s34, 3
	s_mov_b32 s34, 0x222422a
	v_writelane_b32 v57, s34, 4
	s_mov_b32 s34, 0x3a72
	v_writelane_b32 v58, s34, 4
	s_mov_b32 s34, 0x329a1a03
	v_writelane_b32 v57, s34, 5
	s_mov_b32 s34, 0x8a6a
	v_writelane_b32 v58, s34, 5
	s_mov_b32 s34, 0x5b23934b
	v_writelane_b32 v57, s34, 6
	s_mov_b32 s34, 0x3b73
	v_writelane_b32 v58, s34, 6
	s_mov_b32 s34, 0x83541374
	v_writelane_b32 v57, s34, 7
	s_mov_b32 s34, 0x336b
	v_writelane_b32 v58, s34, 7
	s_mov_b32 s34, 0x3c1c2434
	v_writelane_b32 v57, s34, 8
	s_mov_b32 s34, 0x48c
	v_writelane_b32 v58, s34, 8
	s_mov_b32 s34, 0x4c1da455
	v_writelane_b32 v57, s34, 9
	s_mov_b32 s34, 0x449c
	v_writelane_b32 v58, s34, 9
	s_mov_b32 s34, 0x8d25052d
	v_writelane_b32 v57, s34, 10
	s_mov_b32 s34, 0x9d5d
	v_writelane_b32 v58, s34, 10
	s_mov_b32 s34, 0x761e4556
	v_writelane_b32 v57, s34, 11
	s_mov_b32 s34, 0x3565
	v_writelane_b32 v58, s34, 11
	s_mov_b32 s34, 0x46368e6e
	v_writelane_b32 v57, s34, 12
	s_mov_b32 s34, 0x63e
	v_writelane_b32 v58, s34, 12
	s_mov_b32 s34, 0x5f579e77
	v_writelane_b32 v57, s34, 13
	s_mov_b32 s34, 0x2ea6
	v_writelane_b32 v58, s34, 13
	s_mov_b32 s34, 0x174f1f9f
	v_writelane_b32 v57, s34, 14
	s_mov_b32 s34, 0x278f
	v_writelane_b32 v58, s34, 14
	s_mov_b32 s34, 0x38584700
	v_writelane_b32 v57, s34, 15
	s_mov_b32 s34, 0xa897
	v_writelane_b32 v58, s34, 15
	s_mov_b32 s34, 0x90982008
	v_writelane_b32 v57, s34, 16
	s_mov_b32 s34, 0x4060
	v_writelane_b32 v58, s34, 16
	s_mov_b32 s34, 0x411810a1
	v_writelane_b32 v57, s34, 17
	s_mov_b32 s34, 0x5088
	v_writelane_b32 v58, s34, 17
	s_mov_b32 s34, 0x8161197a
	v_writelane_b32 v57, s34, 18
	s_mov_b32 s34, 0x2109
	v_writelane_b32 v58, s34, 18
	s_mov_b32 s34, 0x12314aa2
	v_writelane_b32 v57, s34, 19
	s_mov_b32 s34, 0x1189
	v_writelane_b32 v58, s34, 19
	s_mov_b32 s34, 0x520a430b
	v_writelane_b32 v57, s34, 20
	s_mov_b32 s34, 0x6292
	v_writelane_b32 v58, s34, 20
	s_mov_b32 s34, 0x9b828b53
	v_writelane_b32 v57, s34, 21
	s_mov_b32 s34, 0x2b63
	v_writelane_b32 v58, s34, 21
	s_mov_b32 s34, 0x7c7b5c84
	v_writelane_b32 v57, s34, 22
	s_mov_b32 s34, 0xa31b
	v_writelane_b32 v58, s34, 22
	s_mov_b32 s34, 0x6c0c957d
	v_writelane_b32 v57, s34, 23
	s_mov_b32 s34, 0x942c
	v_writelane_b32 v58, s34, 23
	s_mov_b32 s34, 0x753d85a5
	v_writelane_b32 v57, s34, 24
	s_mov_b32 s34, 0x6414
	v_writelane_b32 v58, s34, 24
	s_mov_b32 s34, 0x5e6d7e26
	v_writelane_b32 v57, s34, 25
	s_mov_b32 s34, 0x4d0d
	v_writelane_b32 v58, s34, 25
	s_mov_b32 s34, 0x8666160f
	v_writelane_b32 v57, s34, 26
	s_mov_b32 s34, 0x9615
	v_writelane_b32 v58, s34, 26
	s_mov_b32 s34, 0x2f7f0787
	v_writelane_b32 v57, s34, 27
	s_mov_b32 s34, 0x4e0e
	v_writelane_b32 v58, s34, 27
	s_mov_b32 s34, 0xa76f2008
	v_writelane_b32 v57, s34, 28
	s_mov_b32 s34, 0x373f
	v_writelane_b32 v58, s34, 28
	s_mov_b32 s34, 0x90982008
	v_writelane_b32 v57, s34, 29
	s_mov_b32 s34, 0x4067
	v_writelane_b32 v58, s34, 29
	s_mov_b32 s34, 0x90982008
	v_writelane_b32 v57, s34, 30
	s_mov_b32 s34, 0x4060
	v_writelane_b32 v58, s34, 30
	s_mov_b32 s34, 0x90982008
	v_writelane_b32 v57, s34, 31
	s_mov_b32 s34, 0x4060
	v_writelane_b32 v58, s34, 31
	s_waitcnt vmcnt(30)
	v_add_f32_e32 v59, 0x3727c5ac, v23
	v_mul_f32_e32 v21, 0x4b800000, v59
	v_cmp_gt_f32_e64 s[6:7], s31, v59
	s_nop 1
	v_cndmask_b32_e64 v59, v59, v21, s[6:7]
	v_rsq_f32_e32 v59, v59
	v_cmp_gt_u32_e64 s[8:9], 3, v26
	v_mul_f32_e32 v2, 0x45800000, v59
	v_cndmask_b32_e64 v2, v59, v2, s[6:7]
	v_mul_f32_e32 v12, v22, v2
	v_cmp_eq_u32_e64 s[6:7], 0, v7
	s_waitcnt vmcnt(29)
	v_fma_mixlo_f16 v2, v12, v25, 0
	s_waitcnt vmcnt(28)
	v_fma_mixlo_f16 v3, v12, v28, 0
	v_cndmask_b32_e64 v8, 0, v3, s[8:9]
	s_waitcnt vmcnt(26)
	v_fma_mixlo_f16 v4, v12, v30, 0
	v_fma_mixlo_f16 v3, v12, v29, 0
	v_cndmask_b32_e64 v2, 0, v2, s[6:7]
	v_cndmask_b32_e32 v4, 0, v4, vcc
	v_cndmask_b32_e64 v3, 0, v3, s[12:13]
	v_pack_b32_f16 v2, v2, v8
	v_lshlrev_b32_e32 v8, 4, v0
	s_waitcnt vmcnt(25)
	v_fma_mixlo_f16 v9, v12, v31, 0
	s_waitcnt vmcnt(24)
	v_fma_mixlo_f16 v10, v12, v32, 0
	v_cndmask_b32_e64 v9, 0, v9, s[14:15]
	v_cndmask_b32_e64 v7, 0, v10, s[16:17]
	v_pack_b32_f16 v4, v4, v7
	v_pack_b32_f16 v3, v3, v9
	v_mov_b32_e32 v9, v5
	global_store_dwordx4 v8, v[2:5], s[24:25]
	v_lshl_add_u64 v[10:11], s[24:25], 0, v[8:9]
	s_waitcnt vmcnt(19)
	v_fma_mixlo_f16 v13, v12, v38, 0
	v_fma_mixlo_f16 v3, v12, v34, 0
	v_fma_mixlo_f16 v4, v12, v36, 0
	v_fma_mixlo_f16 v2, v12, v33, 0
	v_cndmask_b32_e64 v7, 0, v3, s[8:9]
	v_fma_mixlo_f16 v3, v12, v35, 0
	v_cndmask_b32_e64 v9, 0, v4, s[14:15]
	v_fma_mixlo_f16 v4, v12, v37, 0
	v_cndmask_b32_e64 v2, 0, v2, s[6:7]
	v_cndmask_b32_e64 v3, 0, v3, s[12:13]
	v_cndmask_b32_e32 v4, 0, v4, vcc
	v_cndmask_b32_e64 v13, 0, v13, s[16:17]
	v_pack_b32_f16 v4, v4, v13
	v_pack_b32_f16 v3, v3, v9
	v_pack_b32_f16 v2, v2, v7
	global_store_dwordx4 v8, v[2:5], s[24:25] offset:1024
	s_waitcnt vmcnt(14)
	v_fma_mixlo_f16 v13, v12, v44, 0
	v_cndmask_b32_e64 v13, 0, v13, s[16:17]
	v_fma_mixlo_f16 v3, v12, v40, 0
	v_fma_mixlo_f16 v4, v12, v42, 0
	v_fma_mixlo_f16 v2, v12, v39, 0
	v_cndmask_b32_e64 v7, 0, v3, s[8:9]
	v_fma_mixlo_f16 v3, v12, v41, 0
	v_cndmask_b32_e64 v9, 0, v4, s[14:15]
	v_fma_mixlo_f16 v4, v12, v43, 0
	v_cndmask_b32_e64 v2, 0, v2, s[6:7]
	v_cndmask_b32_e64 v3, 0, v3, s[12:13]
	v_cndmask_b32_e32 v4, 0, v4, vcc
	v_pack_b32_f16 v4, v4, v13
	v_pack_b32_f16 v3, v3, v9
	v_pack_b32_f16 v2, v2, v7
	global_store_dwordx4 v8, v[2:5], s[24:25] offset:2048
	s_waitcnt vmcnt(9)
	v_fma_mixlo_f16 v13, v12, v50, 0
	v_cndmask_b32_e64 v13, 0, v13, s[16:17]
	v_fma_mixlo_f16 v3, v12, v45, 0
	v_fma_mixlo_f16 v4, v12, v47, 0
	v_fma_mixlo_f16 v2, v12, v49, 0
	v_cndmask_b32_e64 v7, 0, v3, s[8:9]
	v_fma_mixlo_f16 v3, v12, v46, 0
	v_cndmask_b32_e64 v9, 0, v4, s[14:15]
	v_fma_mixlo_f16 v4, v12, v48, 0
	v_cndmask_b32_e64 v2, 0, v2, s[6:7]
	v_cndmask_b32_e64 v3, 0, v3, s[12:13]
	v_cndmask_b32_e32 v4, 0, v4, vcc
	v_pack_b32_f16 v4, v4, v13
	v_pack_b32_f16 v3, v3, v9
	v_pack_b32_f16 v2, v2, v7
	global_store_dwordx4 v8, v[2:5], s[24:25] offset:3072
	s_and_b64 vcc, s[4:5], vcc
	s_nop 0
	v_and_b32_e32 v2, 35, v0
	s_waitcnt vmcnt(9)
	v_fma_mixlo_f16 v3, v12, v15, 0
	v_cmp_eq_u32_e64 s[6:7], 0, v2
	s_waitcnt vmcnt(6)
	v_fma_mixlo_f16 v4, v12, v18, 0
	v_cndmask_b32_e64 v7, 0, v3, s[6:7]
	v_fma_mixlo_f16 v3, v12, v16, 0
	s_and_b64 s[6:7], s[4:5], s[8:9]
	v_cndmask_b32_e64 v8, 0, v3, s[6:7]
	v_fma_mixlo_f16 v3, v12, v17, 0
	s_and_b64 s[6:7], s[4:5], s[12:13]
	v_cndmask_b32_e64 v3, 0, v3, s[6:7]
	s_and_b64 s[6:7], s[4:5], s[14:15]
	v_cndmask_b32_e64 v9, 0, v4, s[6:7]
	s_waitcnt vmcnt(4)
	v_fma_mixlo_f16 v4, v12, v20, 0
	v_cndmask_b32_e32 v4, 0, v4, vcc
	v_fma_mixlo_f16 v12, v12, v19, 0
	v_cmp_eq_u32_e32 vcc, 3, v2
	v_pack_b32_f16 v3, v3, v9
	s_nop 0
	v_cndmask_b32_e32 v2, 0, v12, vcc
	v_pack_b32_f16 v4, v4, v2
	v_pack_b32_f16 v2, v7, v8
	v_add_co_u32_e32 v8, vcc, 0x1000, v10
	s_nop 1
	v_addc_co_u32_e32 v9, vcc, 0, v11, vcc
	v_cmp_gt_u32_e32 vcc, 8, v0
	global_store_dwordx4 v[8:9], v[2:5], off
	s_and_saveexec_b64 s[4:5], vcc
	s_cbranch_execz .LBB0_7
	s_add_u32 s6, s26, s30
	s_addc_u32 s7, s27, 0
	v_add_f32_e32 v2, 0x3727c5ac, v52
	v_mul_f32_e32 v3, 0x4b800000, v2
	v_cmp_gt_f32_e32 vcc, s31, v2
	s_nop 1
	v_cndmask_b32_e32 v2, v2, v3, vcc
	v_rsq_f32_e32 v2, v2
	v_sub_f32_e32 v3, v53, v54
	v_mul_f32_e32 v4, 0x45800000, v2
	v_cndmask_b32_e32 v2, v2, v4, vcc
	v_mul_f32_e32 v2, v51, v2
	v_fmac_f32_e32 v55, v3, v2
	v_lshlrev_b32_e32 v2, 2, v0
	global_store_dword v2, v55, s[6:7]
